# speedup vs baseline: 1.0048x; 1.0048x over previous
.LBB1_14:
	v_add_u32_e32 v118, s4, v224
	ds_read_b128 v[66:69], v118
	ds_read_b128 v[98:101], v218 offset:8192
	ds_read_b128 v[102:105], v118 offset:32
	ds_read_b128 v[82:85], v118 offset:384
	ds_read_b128 v[86:89], v118 offset:416
	ds_read_b128 v[90:93], v118 offset:448
	ds_read_b128 v[94:97], v118 offset:480
	s_waitcnt lgkmcnt(6)
	v_pk_add_f16 v66, v142, v66
	v_pk_add_f16 v67, v143, v67
	v_pk_add_f16 v68, v144, v68
	v_pk_add_f16 v69, v145, v69
	v_or_b32_e32 v71, 0x80008000, v68
	v_or_b32_e32 v70, 0x80008000, v69
	v_or_b32_e32 v72, 0x80008000, v67
	v_or_b32_e32 v73, 0x80008000, v66
	v_pk_fma_f16 v74, v73, s3, v221 op_sel_hi:[1,0,0]
	v_pk_fma_f16 v75, v72, s3, v221 op_sel_hi:[1,0,0]
	v_pk_fma_f16 v76, v71, s3, v221 op_sel_hi:[1,0,0]
	v_pk_fma_f16 v77, v70, s3, v221 op_sel_hi:[1,0,0]
	v_pk_fma_f16 v76, v76, v71, s20 op_sel_hi:[1,1,0]
	v_pk_fma_f16 v77, v77, v70, s20 op_sel_hi:[1,1,0]
	v_pk_fma_f16 v75, v75, v72, s20 op_sel_hi:[1,1,0]
	v_pk_fma_f16 v74, v74, v73, s20 op_sel_hi:[1,1,0]
	v_pk_fma_f16 v75, v75, v72, s21 op_sel_hi:[1,1,0]
	v_pk_fma_f16 v74, v74, v73, s21 op_sel_hi:[1,1,0]
	v_pk_fma_f16 v76, v76, v71, s21 op_sel_hi:[1,1,0]
	v_pk_fma_f16 v77, v77, v70, s21 op_sel_hi:[1,1,0]
	v_pk_max_f16 v66, v66, 0
	v_exp_f16_e32 v78, v74
	v_exp_f16_e32 v79, v75
	v_exp_f16_e32 v80, v76
	v_exp_f16_e32 v81, v77
	v_exp_f16_sdwa v78, v74 dst_sel:WORD_1 dst_unused:UNUSED_PRESERVE src0_sel:WORD_1
	v_exp_f16_sdwa v79, v75 dst_sel:WORD_1 dst_unused:UNUSED_PRESERVE src0_sel:WORD_1
	v_exp_f16_sdwa v80, v76 dst_sel:WORD_1 dst_unused:UNUSED_PRESERVE src0_sel:WORD_1
	v_exp_f16_sdwa v81, v77 dst_sel:WORD_1 dst_unused:UNUSED_PRESERVE src0_sel:WORD_1
	v_pk_max_f16 v67, v67, 0
	v_pk_max_f16 v68, v68, 0
	v_pk_max_f16 v69, v69, 0
	v_pk_fma_f16 v108, v71, v80, v68
	v_pk_fma_f16 v109, v70, v81, v69
	v_pk_fma_f16 v107, v72, v79, v67
	v_pk_fma_f16 v106, v73, v78, v66
	ds_read_b128 v[66:69], v118 offset:512
	ds_read_b128 v[70:73], v118 offset:544
	ds_read_b128 v[74:77], v118 offset:576
	ds_read_b128 v[78:81], v118 offset:608
	ds_read_b128 v[110:113], v218 offset:9216
	s_waitcnt lgkmcnt(5)
	v_mfma_f32_32x32x16_f16 v[82:97], v[150:153], v[106:109], v[82:97]
	s_waitcnt lgkmcnt(1)
	v_mfma_f32_32x32x16_f16 v[66:81], v[98:101], v[106:109], v[66:81]
	v_pk_add_f16 v98, v146, v102
	v_pk_add_f16 v99, v147, v103
	v_pk_add_f16 v100, v148, v104
	v_pk_add_f16 v101, v149, v105
	v_or_b32_e32 v103, 0x80008000, v100
	v_or_b32_e32 v102, 0x80008000, v101
	v_or_b32_e32 v104, 0x80008000, v99
	v_or_b32_e32 v105, 0x80008000, v98
	v_pk_fma_f16 v106, v105, s3, v221 op_sel_hi:[1,0,0]
	v_pk_fma_f16 v107, v104, s3, v221 op_sel_hi:[1,0,0]
	v_pk_fma_f16 v108, v103, s3, v221 op_sel_hi:[1,0,0]
	v_pk_fma_f16 v109, v102, s3, v221 op_sel_hi:[1,0,0]
	v_pk_fma_f16 v108, v108, v103, s20 op_sel_hi:[1,1,0]
	v_pk_fma_f16 v109, v109, v102, s20 op_sel_hi:[1,1,0]
	v_pk_fma_f16 v107, v107, v104, s20 op_sel_hi:[1,1,0]
	v_pk_fma_f16 v106, v106, v105, s20 op_sel_hi:[1,1,0]
	v_pk_fma_f16 v107, v107, v104, s21 op_sel_hi:[1,1,0]
	v_pk_fma_f16 v106, v106, v105, s21 op_sel_hi:[1,1,0]
	v_pk_fma_f16 v108, v108, v103, s21 op_sel_hi:[1,1,0]
	v_pk_fma_f16 v109, v109, v102, s21 op_sel_hi:[1,1,0]
	v_pk_max_f16 v98, v98, 0
	v_pk_max_f16 v99, v99, 0
	v_pk_max_f16 v100, v100, 0
	v_pk_max_f16 v101, v101, 0
	v_exp_f16_e32 v114, v106
	v_exp_f16_e32 v115, v107
	v_exp_f16_e32 v116, v108
	v_exp_f16_e32 v117, v109
	v_exp_f16_sdwa v114, v106 dst_sel:WORD_1 dst_unused:UNUSED_PRESERVE src0_sel:WORD_1
	v_exp_f16_sdwa v115, v107 dst_sel:WORD_1 dst_unused:UNUSED_PRESERVE src0_sel:WORD_1
	v_exp_f16_sdwa v116, v108 dst_sel:WORD_1 dst_unused:UNUSED_PRESERVE src0_sel:WORD_1
	v_exp_f16_sdwa v117, v109 dst_sel:WORD_1 dst_unused:UNUSED_PRESERVE src0_sel:WORD_1
	s_nop 0
	v_pk_fma_f16 v101, v102, v117, v101
	v_pk_fma_f16 v100, v103, v116, v100
	v_pk_fma_f16 v99, v104, v115, v99
	v_pk_fma_f16 v98, v105, v114, v98
	ds_read_b128 v[102:105], v118 offset:64
	ds_read_b128 v[106:109], v218 offset:2048
	v_mfma_f32_32x32x16_f16 v[82:97], v[154:157], v[98:101], v[82:97]
	v_add_u32_e32 v225, s4, v223
	ds_read_b128 v[126:129], v225
	ds_read_b128 v[130:133], v225 offset:16
	ds_read_b128 v[134:137], v225 offset:32
	ds_read_b128 v[138:141], v225 offset:48
	ds_read_b128 v[150:153], v218 offset:19456
	ds_read_b128 v[154:157], v218 offset:20480
	s_waitcnt lgkmcnt(7)
	v_pk_add_f16 v102, v158, v102
	v_pk_add_f16 v103, v159, v103
	v_pk_add_f16 v104, v160, v104
	v_pk_add_f16 v105, v161, v105
	v_mfma_f32_32x32x16_f16 v[66:81], v[110:113], v[98:101], v[66:81]
	v_or_b32_e32 v110, 0x80008000, v105
	v_or_b32_e32 v111, 0x80008000, v104
	v_or_b32_e32 v112, 0x80008000, v103
	v_or_b32_e32 v113, 0x80008000, v102
	v_pk_fma_f16 v114, v113, s3, v221 op_sel_hi:[1,0,0]
	v_pk_fma_f16 v115, v112, s3, v221 op_sel_hi:[1,0,0]
	v_pk_fma_f16 v116, v111, s3, v221 op_sel_hi:[1,0,0]
	v_pk_fma_f16 v117, v110, s3, v221 op_sel_hi:[1,0,0]
	ds_read_b128 v[98:101], v118 offset:96
	v_pk_fma_f16 v117, v117, v110, s20 op_sel_hi:[1,1,0]
	v_pk_fma_f16 v116, v116, v111, s20 op_sel_hi:[1,1,0]
	v_pk_fma_f16 v115, v115, v112, s20 op_sel_hi:[1,1,0]
	v_pk_fma_f16 v114, v114, v113, s20 op_sel_hi:[1,1,0]
	v_pk_max_f16 v102, v102, 0
	v_pk_max_f16 v103, v103, 0
	v_pk_max_f16 v104, v104, 0
	v_pk_max_f16 v105, v105, 0
	v_pk_fma_f16 v114, v114, v113, s21 op_sel_hi:[1,1,0]
	v_pk_fma_f16 v115, v115, v112, s21 op_sel_hi:[1,1,0]
	v_pk_fma_f16 v116, v116, v111, s21 op_sel_hi:[1,1,0]
	v_pk_fma_f16 v117, v117, v110, s21 op_sel_hi:[1,1,0]
	s_nop 0
	v_exp_f16_e32 v119, v114
	v_exp_f16_e32 v120, v115
	v_exp_f16_e32 v121, v116
	v_exp_f16_e32 v122, v117
	v_exp_f16_sdwa v119, v114 dst_sel:WORD_1 dst_unused:UNUSED_PRESERVE src0_sel:WORD_1
	v_exp_f16_sdwa v120, v115 dst_sel:WORD_1 dst_unused:UNUSED_PRESERVE src0_sel:WORD_1
	v_exp_f16_sdwa v121, v116 dst_sel:WORD_1 dst_unused:UNUSED_PRESERVE src0_sel:WORD_1
	v_exp_f16_sdwa v122, v117 dst_sel:WORD_1 dst_unused:UNUSED_PRESERVE src0_sel:WORD_1
	s_nop 0
	v_pk_fma_f16 v105, v110, v122, v105
	v_pk_fma_f16 v104, v111, v121, v104
	v_pk_fma_f16 v103, v112, v120, v103
	v_pk_fma_f16 v102, v113, v119, v102
	ds_read_b128 v[110:113], v218 offset:3072
	s_waitcnt lgkmcnt(1)
	v_pk_add_f16 v98, v162, v98
	v_mfma_f32_32x32x16_f16 v[82:97], v[106:109], v[102:105], v[82:97]
	ds_read_b128 v[106:109], v218 offset:10240
	ds_read_b128 v[114:117], v218 offset:11264
	v_pk_add_f16 v99, v163, v99
	v_pk_add_f16 v100, v164, v100
	v_pk_add_f16 v101, v165, v101
	s_waitcnt lgkmcnt(1)
	v_mfma_f32_32x32x16_f16 v[66:81], v[106:109], v[102:105], v[66:81]
	v_or_b32_e32 v102, 0x80008000, v101
	v_or_b32_e32 v103, 0x80008000, v100
	v_or_b32_e32 v104, 0x80008000, v99
	v_or_b32_e32 v105, 0x80008000, v98
	v_pk_fma_f16 v106, v105, s3, v221 op_sel_hi:[1,0,0]
	v_pk_fma_f16 v107, v104, s3, v221 op_sel_hi:[1,0,0]
	v_pk_fma_f16 v108, v103, s3, v221 op_sel_hi:[1,0,0]
	v_pk_fma_f16 v109, v102, s3, v221 op_sel_hi:[1,0,0]
	v_pk_fma_f16 v108, v108, v103, s20 op_sel_hi:[1,1,0]
	v_pk_fma_f16 v109, v109, v102, s20 op_sel_hi:[1,1,0]
	v_pk_fma_f16 v107, v107, v104, s20 op_sel_hi:[1,1,0]
	v_pk_fma_f16 v106, v106, v105, s20 op_sel_hi:[1,1,0]
	v_pk_fma_f16 v107, v107, v104, s21 op_sel_hi:[1,1,0]
	v_pk_fma_f16 v106, v106, v105, s21 op_sel_hi:[1,1,0]
	v_pk_fma_f16 v108, v108, v103, s21 op_sel_hi:[1,1,0]
	v_pk_fma_f16 v109, v109, v102, s21 op_sel_hi:[1,1,0]
	v_pk_max_f16 v98, v98, 0
	v_pk_max_f16 v99, v99, 0
	v_pk_max_f16 v100, v100, 0
	v_pk_max_f16 v101, v101, 0
	v_exp_f16_e32 v119, v106
	v_exp_f16_e32 v120, v107
	v_exp_f16_e32 v121, v108
	v_exp_f16_e32 v122, v109
	v_exp_f16_sdwa v119, v106 dst_sel:WORD_1 dst_unused:UNUSED_PRESERVE src0_sel:WORD_1
	v_exp_f16_sdwa v120, v107 dst_sel:WORD_1 dst_unused:UNUSED_PRESERVE src0_sel:WORD_1
	v_exp_f16_sdwa v121, v108 dst_sel:WORD_1 dst_unused:UNUSED_PRESERVE src0_sel:WORD_1
	v_exp_f16_sdwa v122, v109 dst_sel:WORD_1 dst_unused:UNUSED_PRESERVE src0_sel:WORD_1
	s_nop 0
	v_pk_fma_f16 v101, v102, v122, v101
	v_pk_fma_f16 v100, v103, v121, v100
	v_pk_fma_f16 v99, v104, v120, v99
	v_pk_fma_f16 v98, v105, v119, v98
	ds_read_b128 v[102:105], v118 offset:128
	ds_read_b128 v[106:109], v218 offset:4096
	v_mfma_f32_32x32x16_f16 v[82:97], v[110:113], v[98:101], v[82:97]
	s_waitcnt lgkmcnt(1)
	v_pk_add_f16 v102, v166, v102
	v_pk_add_f16 v103, v167, v103
	v_pk_add_f16 v104, v168, v104
	v_pk_add_f16 v105, v169, v105
	v_or_b32_e32 v111, 0x80008000, v104
	v_mfma_f32_32x32x16_f16 v[66:81], v[114:117], v[98:101], v[66:81]
	ds_read_b128 v[226:229], v222
	ds_read_b128 v[230:233], v222 offset:1024
	ds_read_b128 v[234:237], v222 offset:2048
	ds_read_b128 v[238:241], v222 offset:3072
	v_or_b32_e32 v110, 0x80008000, v105
	v_or_b32_e32 v112, 0x80008000, v103
	v_or_b32_e32 v113, 0x80008000, v102
	v_pk_fma_f16 v114, v113, s3, v221 op_sel_hi:[1,0,0]
	v_pk_fma_f16 v115, v112, s3, v221 op_sel_hi:[1,0,0]
	v_pk_fma_f16 v116, v111, s3, v221 op_sel_hi:[1,0,0]
	v_pk_fma_f16 v117, v110, s3, v221 op_sel_hi:[1,0,0]
	ds_read_b128 v[98:101], v118 offset:160
	v_pk_fma_f16 v117, v117, v110, s20 op_sel_hi:[1,1,0]
	v_pk_fma_f16 v116, v116, v111, s20 op_sel_hi:[1,1,0]
	v_pk_fma_f16 v115, v115, v112, s20 op_sel_hi:[1,1,0]
	v_pk_fma_f16 v114, v114, v113, s20 op_sel_hi:[1,1,0]
	v_pk_max_f16 v102, v102, 0
	v_pk_max_f16 v103, v103, 0
	v_pk_max_f16 v104, v104, 0
	v_pk_max_f16 v105, v105, 0
	v_pk_fma_f16 v114, v114, v113, s21 op_sel_hi:[1,1,0]
	v_pk_fma_f16 v115, v115, v112, s21 op_sel_hi:[1,1,0]
	v_pk_fma_f16 v116, v116, v111, s21 op_sel_hi:[1,1,0]
	v_pk_fma_f16 v117, v117, v110, s21 op_sel_hi:[1,1,0]
	s_nop 0
	v_exp_f16_e32 v119, v114
	v_exp_f16_e32 v120, v115
	v_exp_f16_e32 v121, v116
	v_exp_f16_e32 v122, v117
	v_exp_f16_sdwa v119, v114 dst_sel:WORD_1 dst_unused:UNUSED_PRESERVE src0_sel:WORD_1
	v_exp_f16_sdwa v120, v115 dst_sel:WORD_1 dst_unused:UNUSED_PRESERVE src0_sel:WORD_1
	v_exp_f16_sdwa v121, v116 dst_sel:WORD_1 dst_unused:UNUSED_PRESERVE src0_sel:WORD_1
	v_exp_f16_sdwa v122, v117 dst_sel:WORD_1 dst_unused:UNUSED_PRESERVE src0_sel:WORD_1
	s_nop 0
	v_pk_fma_f16 v105, v110, v122, v105
	v_pk_fma_f16 v104, v111, v121, v104
	v_pk_fma_f16 v103, v112, v120, v103
	v_pk_fma_f16 v102, v113, v119, v102
	ds_read_b128 v[110:113], v218 offset:5120
	s_waitcnt lgkmcnt(1)
	v_pk_add_f16 v98, v170, v98
	v_mfma_f32_32x32x16_f16 v[82:97], v[106:109], v[102:105], v[82:97]
	ds_read_b128 v[106:109], v218 offset:12288
	ds_read_b128 v[114:117], v218 offset:13312
	v_pk_add_f16 v99, v171, v99
	v_pk_add_f16 v100, v172, v100
	v_pk_add_f16 v101, v173, v101
	s_waitcnt lgkmcnt(1)
	v_mfma_f32_32x32x16_f16 v[66:81], v[106:109], v[102:105], v[66:81]
	v_or_b32_e32 v102, 0x80008000, v101
	v_or_b32_e32 v103, 0x80008000, v100
	v_or_b32_e32 v104, 0x80008000, v99
	v_or_b32_e32 v105, 0x80008000, v98
	v_pk_fma_f16 v106, v105, s3, v221 op_sel_hi:[1,0,0]
	v_pk_fma_f16 v107, v104, s3, v221 op_sel_hi:[1,0,0]
	v_pk_fma_f16 v108, v103, s3, v221 op_sel_hi:[1,0,0]
	v_pk_fma_f16 v109, v102, s3, v221 op_sel_hi:[1,0,0]
	v_pk_fma_f16 v108, v108, v103, s20 op_sel_hi:[1,1,0]
	v_pk_fma_f16 v109, v109, v102, s20 op_sel_hi:[1,1,0]
	v_pk_fma_f16 v107, v107, v104, s20 op_sel_hi:[1,1,0]
	v_pk_fma_f16 v106, v106, v105, s20 op_sel_hi:[1,1,0]
	v_pk_fma_f16 v107, v107, v104, s21 op_sel_hi:[1,1,0]
	v_pk_fma_f16 v106, v106, v105, s21 op_sel_hi:[1,1,0]
	v_pk_fma_f16 v108, v108, v103, s21 op_sel_hi:[1,1,0]
	v_pk_fma_f16 v109, v109, v102, s21 op_sel_hi:[1,1,0]
	v_pk_max_f16 v98, v98, 0
	v_pk_max_f16 v99, v99, 0
	v_pk_max_f16 v100, v100, 0
	v_pk_max_f16 v101, v101, 0
	v_exp_f16_e32 v119, v106
	v_exp_f16_e32 v120, v107
	v_exp_f16_e32 v121, v108
	v_exp_f16_e32 v122, v109
	v_exp_f16_sdwa v119, v106 dst_sel:WORD_1 dst_unused:UNUSED_PRESERVE src0_sel:WORD_1
	v_exp_f16_sdwa v120, v107 dst_sel:WORD_1 dst_unused:UNUSED_PRESERVE src0_sel:WORD_1
	v_exp_f16_sdwa v121, v108 dst_sel:WORD_1 dst_unused:UNUSED_PRESERVE src0_sel:WORD_1
	v_exp_f16_sdwa v122, v109 dst_sel:WORD_1 dst_unused:UNUSED_PRESERVE src0_sel:WORD_1
	s_nop 0
	v_pk_fma_f16 v101, v102, v122, v101
	v_pk_fma_f16 v100, v103, v121, v100
	v_pk_fma_f16 v99, v104, v120, v99
	v_pk_fma_f16 v98, v105, v119, v98
	ds_read_b128 v[102:105], v118 offset:192
	ds_read_b128 v[106:109], v218 offset:6144
	v_mfma_f32_32x32x16_f16 v[82:97], v[110:113], v[98:101], v[82:97]
	s_waitcnt lgkmcnt(1)
	v_pk_add_f16 v102, v174, v102
	v_pk_add_f16 v103, v175, v103
	v_pk_add_f16 v104, v176, v104
	v_pk_add_f16 v105, v177, v105
	v_or_b32_e32 v111, 0x80008000, v104
	v_mfma_f32_32x32x16_f16 v[66:81], v[114:117], v[98:101], v[66:81]
	v_or_b32_e32 v110, 0x80008000, v105
	v_or_b32_e32 v112, 0x80008000, v103
	v_or_b32_e32 v113, 0x80008000, v102
	v_pk_fma_f16 v114, v113, s3, v221 op_sel_hi:[1,0,0]
	v_pk_fma_f16 v115, v112, s3, v221 op_sel_hi:[1,0,0]
	v_pk_fma_f16 v116, v111, s3, v221 op_sel_hi:[1,0,0]
	v_pk_fma_f16 v117, v110, s3, v221 op_sel_hi:[1,0,0]
	ds_read_b128 v[98:101], v118 offset:224
	v_pk_fma_f16 v117, v117, v110, s20 op_sel_hi:[1,1,0]
	v_pk_fma_f16 v116, v116, v111, s20 op_sel_hi:[1,1,0]
	v_pk_fma_f16 v115, v115, v112, s20 op_sel_hi:[1,1,0]
	v_pk_fma_f16 v114, v114, v113, s20 op_sel_hi:[1,1,0]
	v_pk_max_f16 v102, v102, 0
	v_pk_max_f16 v103, v103, 0
	v_pk_max_f16 v104, v104, 0
	v_pk_max_f16 v105, v105, 0
	v_pk_fma_f16 v114, v114, v113, s21 op_sel_hi:[1,1,0]
	v_pk_fma_f16 v115, v115, v112, s21 op_sel_hi:[1,1,0]
	v_pk_fma_f16 v116, v116, v111, s21 op_sel_hi:[1,1,0]
	v_pk_fma_f16 v117, v117, v110, s21 op_sel_hi:[1,1,0]
	s_waitcnt lgkmcnt(0)
	v_pk_add_f16 v98, v178, v98
	ds_read_b128 v[242:245], v218 offset:16384
	ds_read_b128 v[246:249], v218 offset:17408
	ds_read_b128 v[250:253], v218 offset:18432
	v_exp_f16_e32 v118, v114
	v_exp_f16_e32 v119, v115
	v_exp_f16_e32 v120, v116
	v_exp_f16_e32 v121, v117
	v_exp_f16_sdwa v118, v114 dst_sel:WORD_1 dst_unused:UNUSED_PRESERVE src0_sel:WORD_1
	v_exp_f16_sdwa v119, v115 dst_sel:WORD_1 dst_unused:UNUSED_PRESERVE src0_sel:WORD_1
	v_exp_f16_sdwa v120, v116 dst_sel:WORD_1 dst_unused:UNUSED_PRESERVE src0_sel:WORD_1
	v_exp_f16_sdwa v121, v117 dst_sel:WORD_1 dst_unused:UNUSED_PRESERVE src0_sel:WORD_1
	v_pk_add_f16 v99, v179, v99
	v_pk_fma_f16 v105, v110, v121, v105
	v_pk_fma_f16 v104, v111, v120, v104
	v_pk_fma_f16 v103, v112, v119, v103
	v_pk_fma_f16 v102, v113, v118, v102
	ds_read_b128 v[110:113], v218 offset:7168
	v_pk_add_f16 v100, v180, v100
	v_mfma_f32_32x32x16_f16 v[82:97], v[106:109], v[102:105], v[82:97]
	ds_read_b128 v[106:109], v218 offset:14336
	ds_read_b128 v[114:117], v218 offset:15360
	v_pk_add_f16 v101, v181, v101
	s_waitcnt lgkmcnt(1)
	v_mfma_f32_32x32x16_f16 v[66:81], v[106:109], v[102:105], v[66:81]
	v_or_b32_e32 v102, 0x80008000, v101
	v_or_b32_e32 v103, 0x80008000, v100
	v_or_b32_e32 v104, 0x80008000, v99
	v_or_b32_e32 v105, 0x80008000, v98
	v_pk_fma_f16 v106, v105, s3, v221 op_sel_hi:[1,0,0]
	v_pk_fma_f16 v107, v104, s3, v221 op_sel_hi:[1,0,0]
	v_pk_fma_f16 v108, v103, s3, v221 op_sel_hi:[1,0,0]
	v_pk_fma_f16 v109, v102, s3, v221 op_sel_hi:[1,0,0]
	v_pk_fma_f16 v108, v108, v103, s20 op_sel_hi:[1,1,0]
	v_pk_fma_f16 v109, v109, v102, s20 op_sel_hi:[1,1,0]
	v_pk_fma_f16 v107, v107, v104, s20 op_sel_hi:[1,1,0]
	v_pk_fma_f16 v106, v106, v105, s20 op_sel_hi:[1,1,0]
	v_pk_max_f16 v98, v98, 0
	v_pk_max_f16 v99, v99, 0
	v_pk_max_f16 v100, v100, 0
	v_pk_max_f16 v101, v101, 0
	v_pk_fma_f16 v106, v106, v105, s21 op_sel_hi:[1,1,0]
	v_pk_fma_f16 v107, v107, v104, s21 op_sel_hi:[1,1,0]
	v_pk_fma_f16 v108, v108, v103, s21 op_sel_hi:[1,1,0]
	v_pk_fma_f16 v109, v109, v102, s21 op_sel_hi:[1,1,0]
	s_nop 0
	v_exp_f16_e32 v118, v106
	v_exp_f16_e32 v119, v107
	v_exp_f16_e32 v120, v108
	v_exp_f16_e32 v121, v109
	v_exp_f16_sdwa v118, v106 dst_sel:WORD_1 dst_unused:UNUSED_PRESERVE src0_sel:WORD_1
	v_exp_f16_sdwa v119, v107 dst_sel:WORD_1 dst_unused:UNUSED_PRESERVE src0_sel:WORD_1
	v_exp_f16_sdwa v120, v108 dst_sel:WORD_1 dst_unused:UNUSED_PRESERVE src0_sel:WORD_1
	v_exp_f16_sdwa v121, v109 dst_sel:WORD_1 dst_unused:UNUSED_PRESERVE src0_sel:WORD_1
	s_nop 0
	v_pk_fma_f16 v101, v102, v121, v101
	v_pk_fma_f16 v100, v103, v120, v100
	v_pk_fma_f16 v99, v104, v119, v99
	v_pk_fma_f16 v98, v105, v118, v98
	s_nop 1
	v_mfma_f32_32x32x16_f16 v[82:97], v[110:113], v[98:101], v[82:97]
	s_waitcnt lgkmcnt(0)
	v_mfma_f32_32x32x16_f16 v[66:81], v[114:117], v[98:101], v[66:81]
	s_setprio 1
	ds_read_b128 v[98:101], v222 offset:4096
	ds_read_b128 v[102:105], v222 offset:5120
	ds_read_b128 v[106:109], v222 offset:6144
	ds_read_b128 v[110:113], v222 offset:7168
	s_nop 4
	v_cvt_pk_f16_f32 v114, v82, v83
	v_cvt_pk_f16_f32 v115, v84, v85
	v_cvt_pk_f16_f32 v116, v86, v87
	v_cvt_pk_f16_f32 v117, v88, v89
	v_pk_add_f16 v126, v126, v114
	v_pk_add_f16 v127, v127, v115
	v_pk_add_f16 v128, v128, v116
	v_pk_add_f16 v129, v129, v117
	s_nop 1
	v_mfma_f32_32x32x16_f16 v[226:241], v[242:245], v[126:129], v[226:241]
	ds_read_b128 v[242:245], v218 offset:21504
	v_cvt_pk_f16_f32 v118, v90, v91
	v_cvt_pk_f16_f32 v119, v92, v93
	v_cvt_pk_f16_f32 v120, v94, v95
	v_cvt_pk_f16_f32 v121, v96, v97
	v_pk_add_f16 v130, v130, v118
	v_pk_add_f16 v131, v131, v119
	v_pk_add_f16 v132, v132, v120
	v_pk_add_f16 v133, v133, v121
	s_nop 1
	v_mfma_f32_32x32x16_f16 v[226:241], v[246:249], v[130:133], v[226:241]
	ds_read_b128 v[246:249], v218 offset:22528
	v_cvt_pk_f16_f32 v122, v66, v67
	v_cvt_pk_f16_f32 v123, v68, v69
	v_cvt_pk_f16_f32 v124, v70, v71
	v_cvt_pk_f16_f32 v125, v72, v73
	v_pk_add_f16 v134, v134, v122
	v_pk_add_f16 v135, v135, v123
	v_pk_add_f16 v136, v136, v124
	v_pk_add_f16 v137, v137, v125
	s_nop 1
	v_mfma_f32_32x32x16_f16 v[226:241], v[250:253], v[134:137], v[226:241]
	ds_read_b128 v[250:253], v218 offset:23552
	v_cvt_pk_f16_f32 v182, v74, v75
	v_cvt_pk_f16_f32 v183, v76, v77
	v_cvt_pk_f16_f32 v184, v78, v79
	v_cvt_pk_f16_f32 v185, v80, v81
	v_pk_add_f16 v138, v138, v182
	v_pk_add_f16 v139, v139, v183
	v_pk_add_f16 v140, v140, v184
	v_pk_add_f16 v141, v141, v185
	s_nop 1
	v_mfma_f32_32x32x16_f16 v[226:241], v[150:153], v[138:141], v[226:241]
	ds_read_b128 v[150:153], v218 offset:24576
	ds_read_b128 v[66:69], v222 offset:8192
	ds_read_b128 v[70:73], v222 offset:9216
	ds_read_b128 v[74:77], v222 offset:10240
	ds_read_b128 v[78:81], v222 offset:11264
	ds_read_b128 v[82:85], v222 offset:12288
	ds_read_b128 v[86:89], v222 offset:13312
	ds_read_b128 v[90:93], v222 offset:14336
	ds_read_b128 v[94:97], v222 offset:15360
	s_waitcnt lgkmcnt(12)
	v_mfma_f32_32x32x16_f16 v[98:113], v[154:157], v[126:129], v[98:113]
	ds_read_b128 v[154:157], v218 offset:25600
	s_waitcnt lgkmcnt(12)
	v_mfma_f32_32x32x16_f16 v[98:113], v[242:245], v[130:133], v[98:113]
	ds_read_b128 v[242:245], v218 offset:26624
	s_waitcnt lgkmcnt(12)
	v_mfma_f32_32x32x16_f16 v[98:113], v[246:249], v[134:137], v[98:113]
	ds_read_b128 v[246:249], v218 offset:27648
	v_cvt_pk_f16_f32 v226, v226, v227
	v_cvt_pk_f16_f32 v227, v228, v229
	v_cvt_pk_f16_f32 v228, v230, v231
	v_cvt_pk_f16_f32 v229, v232, v233
	v_pk_max_f16 v226, v226, 0
	v_pk_max_f16 v227, v227, 0
	v_pk_max_f16 v228, v228, 0
	v_pk_max_f16 v229, v229, 0
	s_waitcnt lgkmcnt(12)
	v_mfma_f32_32x32x16_f16 v[98:113], v[250:253], v[138:141], v[98:113]
	ds_read_b128 v[250:253], v218 offset:28672
	v_cvt_pk_f16_f32 v230, v234, v235
	v_cvt_pk_f16_f32 v231, v236, v237
	v_cvt_pk_f16_f32 v232, v238, v239
	v_cvt_pk_f16_f32 v233, v240, v241
	v_pk_max_f16 v230, v230, 0
	v_pk_max_f16 v231, v231, 0
	v_pk_max_f16 v232, v232, 0
	v_pk_max_f16 v233, v233, 0
	s_waitcnt lgkmcnt(8)
	v_mfma_f32_32x32x16_f16 v[66:81], v[150:153], v[126:129], v[66:81]
	ds_read_b128 v[150:153], v218 offset:29696
	s_waitcnt lgkmcnt(4)
	v_mfma_f32_32x32x16_f16 v[66:81], v[154:157], v[130:133], v[66:81]
	ds_read_b128 v[154:157], v218 offset:30720
	s_waitcnt lgkmcnt(4)
	v_mfma_f32_32x32x16_f16 v[66:81], v[242:245], v[134:137], v[66:81]
	ds_read_b128 v[242:245], v218 offset:31744
	v_cvt_pk_f16_f32 v98, v98, v99
	v_cvt_pk_f16_f32 v99, v100, v101
	v_cvt_pk_f16_f32 v100, v102, v103
	v_cvt_pk_f16_f32 v101, v104, v105
	v_pk_max_f16 v98, v98, 0
	v_pk_max_f16 v99, v99, 0
	v_pk_max_f16 v100, v100, 0
	v_pk_max_f16 v101, v101, 0
	s_waitcnt lgkmcnt(4)
	v_mfma_f32_32x32x16_f16 v[66:81], v[246:249], v[138:141], v[66:81]
	ds_read_b128 v[246:249], v218 offset:32768
	v_cvt_pk_f16_f32 v102, v106, v107
	v_cvt_pk_f16_f32 v103, v108, v109
	v_cvt_pk_f16_f32 v104, v110, v111
	v_cvt_pk_f16_f32 v105, v112, v113
	v_pk_max_f16 v102, v102, 0
	v_pk_max_f16 v103, v103, 0
	v_pk_max_f16 v104, v104, 0
	v_pk_max_f16 v105, v105, 0
	s_waitcnt lgkmcnt(4)
	v_mfma_f32_32x32x16_f16 v[82:97], v[250:253], v[126:129], v[82:97]
	ds_read_b128 v[250:253], v218 offset:33792
	s_waitcnt lgkmcnt(4)
	v_mfma_f32_32x32x16_f16 v[82:97], v[150:153], v[130:133], v[82:97]
	ds_read_b128 v[150:153], v218 offset:34816
	s_waitcnt lgkmcnt(4)
	v_mfma_f32_32x32x16_f16 v[82:97], v[154:157], v[134:137], v[82:97]
	ds_read_b128 v[154:157], v218 offset:35840
	v_cvt_pk_f16_f32 v66, v66, v67
	v_cvt_pk_f16_f32 v67, v68, v69
	v_cvt_pk_f16_f32 v68, v70, v71
	v_cvt_pk_f16_f32 v69, v72, v73
	v_pk_max_f16 v66, v66, 0
	v_pk_max_f16 v67, v67, 0
	v_pk_max_f16 v68, v68, 0
	v_pk_max_f16 v69, v69, 0
	s_waitcnt lgkmcnt(4)
	v_mfma_f32_32x32x16_f16 v[82:97], v[242:245], v[138:141], v[82:97]
	ds_read_b128 v[242:245], v218 offset:36864
	v_cvt_pk_f16_f32 v70, v74, v75
	v_cvt_pk_f16_f32 v71, v76, v77
	v_cvt_pk_f16_f32 v72, v78, v79
	v_cvt_pk_f16_f32 v73, v80, v81
	v_pk_max_f16 v70, v70, 0
	v_pk_max_f16 v71, v71, 0
	v_pk_max_f16 v72, v72, 0
	v_pk_max_f16 v73, v73, 0
	s_waitcnt lgkmcnt(4)
	v_mfma_f32_32x32x16_f16 v[126:141], v[246:249], v[226:229], v[2:17]
	ds_read_b128 v[246:249], v218 offset:37888
	s_waitcnt lgkmcnt(4)
	v_mfma_f32_32x32x16_f16 v[126:141], v[250:253], v[230:233], v[126:141]
	ds_read_b128 v[250:253], v218 offset:38912
	s_waitcnt lgkmcnt(4)
	v_mfma_f32_32x32x16_f16 v[126:141], v[150:153], v[98:101], v[126:141]
	ds_read_b128 v[150:153], v218 offset:39936
	s_waitcnt lgkmcnt(4)
	v_mfma_f32_32x32x16_f16 v[126:141], v[154:157], v[102:105], v[126:141]
	ds_read_b128 v[154:157], v218 offset:40960
	s_waitcnt lgkmcnt(4)
	v_mfma_f32_32x32x16_f16 v[126:141], v[242:245], v[66:69], v[126:141]
	ds_read_b128 v[242:245], v218 offset:41984
	v_cvt_pk_f16_f32 v97, v96, v97
	v_cvt_pk_f16_f32 v96, v94, v95
	v_cvt_pk_f16_f32 v95, v92, v93
	v_cvt_pk_f16_f32 v94, v90, v91
	v_pk_max_f16 v97, v97, 0
	v_pk_max_f16 v96, v96, 0
	v_pk_max_f16 v95, v95, 0
	v_pk_max_f16 v94, v94, 0
	s_waitcnt lgkmcnt(4)
	v_mfma_f32_32x32x16_f16 v[126:141], v[246:249], v[70:73], v[126:141]
	ds_read_b128 v[246:249], v218 offset:43008
	v_cvt_pk_f16_f32 v93, v88, v89
	v_cvt_pk_f16_f32 v92, v86, v87
	v_cvt_pk_f16_f32 v91, v84, v85
	v_cvt_pk_f16_f32 v90, v82, v83
	v_pk_max_f16 v93, v93, 0
	v_pk_max_f16 v92, v92, 0
	v_pk_max_f16 v91, v91, 0
	v_pk_max_f16 v90, v90, 0
	s_waitcnt lgkmcnt(4)
	s_nop 0
	v_mfma_f32_32x32x16_f16 v[126:141], v[250:253], v[90:93], v[126:141]
	ds_read_b128 v[250:253], v218 offset:44032
	s_waitcnt lgkmcnt(4)
	v_mfma_f32_32x32x16_f16 v[126:141], v[150:153], v[94:97], v[126:141]
	ds_read_b128 v[150:153], v218 offset:45056
	s_waitcnt lgkmcnt(4)
	v_mfma_f32_32x32x16_f16 v[74:89], v[154:157], v[226:229], v[34:49]
	ds_read_b128 v[154:157], v218 offset:46080
	s_waitcnt lgkmcnt(4)
	v_mfma_f32_32x32x16_f16 v[74:89], v[242:245], v[230:233], v[74:89]
	ds_read_b128 v[242:245], v218 offset:47104
	s_waitcnt lgkmcnt(4)
	v_mfma_f32_32x32x16_f16 v[74:89], v[246:249], v[98:101], v[74:89]
	ds_read_b128 v[246:249], v218 offset:48128
	s_waitcnt lgkmcnt(4)
	v_mfma_f32_32x32x16_f16 v[74:89], v[250:253], v[102:105], v[74:89]
	s_waitcnt lgkmcnt(3)
	v_mfma_f32_32x32x16_f16 v[74:89], v[150:153], v[66:69], v[74:89]
	ds_read_b128 v[150:153], v218
	v_max3_f32 v254, v126, v127, v128
	v_max3_f32 v255, v129, v130, v131
	v_max3_f32 v254, v254, v132, v133
	v_max3_f32 v255, v255, v134, v135
	v_max3_f32 v254, v254, v136, v137
	v_max3_f32 v255, v255, v138, v139
	v_max3_f32 v254, v254, v140, v141
	v_max_f32_e32 v254, v254, v255
	v_cmp_lt_f32_e32 vcc, s5, v254
	s_cbranch_vccz .Lm_norescale0
	v_max_f32_e32 v234, 0, v126
	v_max_f32_e32 v235, 0, v127
	v_max_f32_e32 v236, 0, v128
	v_max_f32_e32 v237, 0, v129
	v_max_f32_e32 v238, 0, v130
	v_max_f32_e32 v239, 0, v131
	v_max_f32_e32 v240, 0, v132
	v_max_f32_e32 v241, 0, v133
	v_max_f32_e32 v106, 0, v134
	v_max_f32_e32 v107, 0, v135
	v_max_f32_e32 v108, 0, v136
	v_max_f32_e32 v109, 0, v137
	v_max_f32_e32 v110, 0, v138
	v_max_f32_e32 v111, 0, v139
	v_max_f32_e32 v112, 0, v140
	v_max_f32_e32 v113, 0, v141
	v_sub_f32_e32 v126, v126, v234
	v_sub_f32_e32 v127, v127, v235
	v_sub_f32_e32 v128, v128, v236
	v_sub_f32_e32 v129, v129, v237
	v_sub_f32_e32 v130, v130, v238
	v_sub_f32_e32 v131, v131, v239
	v_sub_f32_e32 v132, v132, v240
	v_sub_f32_e32 v133, v133, v241
	v_sub_f32_e32 v134, v134, v106
	v_sub_f32_e32 v135, v135, v107
	v_sub_f32_e32 v136, v136, v108
	v_sub_f32_e32 v137, v137, v109
	v_sub_f32_e32 v138, v138, v110
	v_sub_f32_e32 v139, v139, v111
	v_sub_f32_e32 v140, v140, v112
	v_sub_f32_e32 v141, v141, v113
	v_sub_f32_e32 v2, v2, v234
	v_sub_f32_e32 v3, v3, v235
	v_sub_f32_e32 v4, v4, v236
	v_sub_f32_e32 v5, v5, v237
	v_sub_f32_e32 v6, v6, v238
	v_sub_f32_e32 v7, v7, v239
	v_sub_f32_e32 v8, v8, v240
	v_sub_f32_e32 v9, v9, v241
	v_sub_f32_e32 v10, v10, v106
	v_sub_f32_e32 v11, v11, v107
	v_sub_f32_e32 v12, v12, v108
	v_sub_f32_e32 v13, v13, v109
	v_sub_f32_e32 v14, v14, v110
	v_sub_f32_e32 v15, v15, v111
	v_sub_f32_e32 v16, v16, v112
	v_sub_f32_e32 v17, v17, v113
	v_exp_f32_e64 v234, -v234
	v_exp_f32_e64 v235, -v235
	v_exp_f32_e64 v236, -v236
	v_exp_f32_e64 v237, -v237
	v_exp_f32_e64 v238, -v238
	v_exp_f32_e64 v239, -v239
	v_exp_f32_e64 v240, -v240
	v_exp_f32_e64 v241, -v241
	v_exp_f32_e64 v106, -v106
	v_exp_f32_e64 v107, -v107
	v_exp_f32_e64 v108, -v108
	v_exp_f32_e64 v109, -v109
	v_exp_f32_e64 v110, -v110
	v_exp_f32_e64 v111, -v111
	v_exp_f32_e64 v112, -v112
	v_exp_f32_e64 v113, -v113
	s_nop 0
	v_mul_f32_e32 v50, v234, v50
	v_mul_f32_e32 v51, v235, v51
	v_mul_f32_e32 v52, v236, v52
	v_mul_f32_e32 v53, v237, v53
	v_mul_f32_e32 v54, v238, v54
	v_mul_f32_e32 v55, v239, v55
	v_mul_f32_e32 v56, v240, v56
	v_mul_f32_e32 v57, v241, v57
	v_mul_f32_e32 v58, v106, v58
	v_mul_f32_e32 v59, v107, v59
	v_mul_f32_e32 v60, v108, v60
	v_mul_f32_e32 v61, v109, v61
	v_mul_f32_e32 v62, v110, v62
	v_mul_f32_e32 v63, v111, v63
	v_mul_f32_e32 v64, v112, v64
	v_mul_f32_e32 v65, v113, v65
	v_mul_f32_e32 v216, v234, v216
	v_mul_f32_e32 v217, v235, v217
	v_mul_f32_e32 v214, v236, v214
	v_mul_f32_e32 v215, v237, v215
	v_mul_f32_e32 v212, v238, v212
	v_mul_f32_e32 v213, v239, v213
	v_mul_f32_e32 v210, v240, v210
	v_mul_f32_e32 v211, v241, v211
	v_mul_f32_e32 v208, v106, v208
	v_mul_f32_e32 v209, v107, v209
	v_mul_f32_e32 v204, v108, v204
	v_mul_f32_e32 v205, v109, v205
	v_mul_f32_e32 v202, v110, v202
	v_mul_f32_e32 v203, v111, v203
	v_mul_f32_e32 v196, v112, v196
	v_mul_f32_e32 v197, v113, v197
	s_nop 1
.Lm_norescale0:
	s_waitcnt lgkmcnt(3)
	v_mfma_f32_32x32x16_f16 v[74:89], v[154:157], v[70:73], v[74:89]
	ds_read_b128 v[154:157], v218 offset:1024
	v_exp_f32_e32 v234, v126
	v_exp_f32_e32 v235, v127
	v_exp_f32_e32 v236, v128
	v_exp_f32_e32 v237, v129
	v_exp_f32_e32 v238, v130
	v_exp_f32_e32 v239, v131
	v_exp_f32_e32 v240, v132
	v_exp_f32_e32 v241, v133
	s_waitcnt lgkmcnt(3)
	v_mfma_f32_32x32x16_f16 v[74:89], v[242:245], v[90:93], v[74:89]
	v_exp_f32_e32 v106, v134
	v_exp_f32_e32 v107, v135
	v_exp_f32_e32 v108, v136
	v_exp_f32_e32 v109, v137
	v_exp_f32_e32 v110, v138
	v_exp_f32_e32 v111, v139
	v_exp_f32_e32 v112, v140
	v_exp_f32_e32 v113, v141
	v_pk_add_f32 v[50:51], v[234:235], v[50:51]
	v_pk_add_f32 v[52:53], v[236:237], v[52:53]
	v_pk_add_f32 v[54:55], v[238:239], v[54:55]
	v_pk_add_f32 v[56:57], v[240:241], v[56:57]
	s_waitcnt lgkmcnt(2)
	v_mfma_f32_32x32x16_f16 v[74:89], v[246:249], v[94:97], v[74:89]
	v_pk_add_f32 v[58:59], v[106:107], v[58:59]
	v_pk_add_f32 v[60:61], v[108:109], v[60:61]
	v_pk_add_f32 v[62:63], v[110:111], v[62:63]
	v_pk_add_f32 v[64:65], v[112:113], v[64:65]
	v_fma_mix_f32 v216, v234, v114, v216 op_sel:[0,0,0] op_sel_hi:[0,1,0]
	v_fma_mix_f32 v217, v235, v114, v217 op_sel:[0,1,0] op_sel_hi:[0,1,0]
	v_fma_mix_f32 v214, v236, v115, v214 op_sel:[0,0,0] op_sel_hi:[0,1,0]
	v_fma_mix_f32 v215, v237, v115, v215 op_sel:[0,1,0] op_sel_hi:[0,1,0]
	v_fma_mix_f32 v212, v238, v116, v212 op_sel:[0,0,0] op_sel_hi:[0,1,0]
	v_fma_mix_f32 v213, v239, v116, v213 op_sel:[0,1,0] op_sel_hi:[0,1,0]
	v_fma_mix_f32 v210, v240, v117, v210 op_sel:[0,0,0] op_sel_hi:[0,1,0]
	v_fma_mix_f32 v211, v241, v117, v211 op_sel:[0,1,0] op_sel_hi:[0,1,0]
	v_fma_mix_f32 v208, v106, v118, v208 op_sel:[0,0,0] op_sel_hi:[0,1,0]
	v_fma_mix_f32 v209, v107, v118, v209 op_sel:[0,1,0] op_sel_hi:[0,1,0]
	v_fma_mix_f32 v204, v108, v119, v204 op_sel:[0,0,0] op_sel_hi:[0,1,0]
	v_fma_mix_f32 v205, v109, v119, v205 op_sel:[0,1,0] op_sel_hi:[0,1,0]
	v_fma_mix_f32 v202, v110, v120, v202 op_sel:[0,0,0] op_sel_hi:[0,1,0]
	v_fma_mix_f32 v203, v111, v120, v203 op_sel:[0,1,0] op_sel_hi:[0,1,0]
	v_fma_mix_f32 v196, v112, v121, v196 op_sel:[0,0,0] op_sel_hi:[0,1,0]
	v_fma_mix_f32 v197, v113, v121, v197 op_sel:[0,1,0] op_sel_hi:[0,1,0]
	v_max3_f32 v254, v74, v75, v76
	v_max3_f32 v255, v77, v78, v79
	v_max3_f32 v254, v254, v80, v81
	v_max3_f32 v255, v255, v82, v83
	v_max3_f32 v254, v254, v84, v85
	v_max3_f32 v255, v255, v86, v87
	v_max3_f32 v254, v254, v88, v89
	v_max_f32_e32 v254, v254, v255
	v_cmp_lt_f32_e32 vcc, s5, v254
	s_cbranch_vccz .Lm_norescale1
	v_max_f32_e32 v234, 0, v74
	v_max_f32_e32 v235, 0, v75
	v_max_f32_e32 v236, 0, v76
	v_max_f32_e32 v237, 0, v77
	v_max_f32_e32 v238, 0, v78
	v_max_f32_e32 v239, 0, v79
	v_max_f32_e32 v240, 0, v80
	v_max_f32_e32 v241, 0, v81
	v_max_f32_e32 v106, 0, v82
	v_max_f32_e32 v107, 0, v83
	v_max_f32_e32 v108, 0, v84
	v_max_f32_e32 v109, 0, v85
	v_max_f32_e32 v110, 0, v86
	v_max_f32_e32 v111, 0, v87
	v_max_f32_e32 v112, 0, v88
	v_max_f32_e32 v113, 0, v89
	v_sub_f32_e32 v74, v74, v234
	v_sub_f32_e32 v75, v75, v235
	v_sub_f32_e32 v76, v76, v236
	v_sub_f32_e32 v77, v77, v237
	v_sub_f32_e32 v78, v78, v238
	v_sub_f32_e32 v79, v79, v239
	v_sub_f32_e32 v80, v80, v240
	v_sub_f32_e32 v81, v81, v241
	v_sub_f32_e32 v82, v82, v106
	v_sub_f32_e32 v83, v83, v107
	v_sub_f32_e32 v84, v84, v108
	v_sub_f32_e32 v85, v85, v109
	v_sub_f32_e32 v86, v86, v110
	v_sub_f32_e32 v87, v87, v111
	v_sub_f32_e32 v88, v88, v112
	v_sub_f32_e32 v89, v89, v113
	v_sub_f32_e32 v34, v34, v234
	v_sub_f32_e32 v35, v35, v235
	v_sub_f32_e32 v36, v36, v236
	v_sub_f32_e32 v37, v37, v237
	v_sub_f32_e32 v38, v38, v238
	v_sub_f32_e32 v39, v39, v239
	v_sub_f32_e32 v40, v40, v240
	v_sub_f32_e32 v41, v41, v241
	v_sub_f32_e32 v42, v42, v106
	v_sub_f32_e32 v43, v43, v107
	v_sub_f32_e32 v44, v44, v108
	v_sub_f32_e32 v45, v45, v109
	v_sub_f32_e32 v46, v46, v110
	v_sub_f32_e32 v47, v47, v111
	v_sub_f32_e32 v48, v48, v112
	v_sub_f32_e32 v49, v49, v113
	v_exp_f32_e64 v234, -v234
	v_exp_f32_e64 v235, -v235
	v_exp_f32_e64 v236, -v236
	v_exp_f32_e64 v237, -v237
	v_exp_f32_e64 v238, -v238
	v_exp_f32_e64 v239, -v239
	v_exp_f32_e64 v240, -v240
	v_exp_f32_e64 v241, -v241
	v_exp_f32_e64 v106, -v106
	v_exp_f32_e64 v107, -v107
	v_exp_f32_e64 v108, -v108
	v_exp_f32_e64 v109, -v109
	v_exp_f32_e64 v110, -v110
	v_exp_f32_e64 v111, -v111
	v_exp_f32_e64 v112, -v112
	v_exp_f32_e64 v113, -v113
	s_nop 0
	v_mul_f32_e32 v18, v234, v18
	v_mul_f32_e32 v19, v235, v19
	v_mul_f32_e32 v20, v236, v20
	v_mul_f32_e32 v21, v237, v21
	v_mul_f32_e32 v22, v238, v22
	v_mul_f32_e32 v23, v239, v23
	v_mul_f32_e32 v24, v240, v24
	v_mul_f32_e32 v25, v241, v25
	v_mul_f32_e32 v26, v106, v26
	v_mul_f32_e32 v27, v107, v27
	v_mul_f32_e32 v28, v108, v28
	v_mul_f32_e32 v29, v109, v29
	v_mul_f32_e32 v30, v110, v30
	v_mul_f32_e32 v31, v111, v31
	v_mul_f32_e32 v32, v112, v32
	v_mul_f32_e32 v33, v113, v33
	v_mul_f32_e32 v206, v234, v206
	v_mul_f32_e32 v207, v235, v207
	v_mul_f32_e32 v200, v236, v200
	v_mul_f32_e32 v201, v237, v201
	v_mul_f32_e32 v198, v238, v198
	v_mul_f32_e32 v199, v239, v199
	v_mul_f32_e32 v194, v240, v194
	v_mul_f32_e32 v195, v241, v195
	v_mul_f32_e32 v192, v106, v192
	v_mul_f32_e32 v193, v107, v193
	v_mul_f32_e32 v190, v108, v190
	v_mul_f32_e32 v191, v109, v191
	v_mul_f32_e32 v188, v110, v188
	v_mul_f32_e32 v189, v111, v189
	v_mul_f32_e32 v186, v112, v186
	v_mul_f32_e32 v187, v113, v187
	s_nop 1
.Lm_norescale1:
	v_exp_f32_e32 v234, v74
	v_exp_f32_e32 v235, v75
	v_exp_f32_e32 v236, v76
	v_exp_f32_e32 v237, v77
	v_exp_f32_e32 v238, v78
	v_exp_f32_e32 v239, v79
	v_exp_f32_e32 v240, v80
	v_exp_f32_e32 v241, v81
	v_exp_f32_e32 v106, v82
	v_exp_f32_e32 v107, v83
	v_exp_f32_e32 v108, v84
	v_exp_f32_e32 v109, v85
	v_exp_f32_e32 v110, v86
	v_exp_f32_e32 v111, v87
	v_exp_f32_e32 v112, v88
	v_exp_f32_e32 v113, v89
	v_pk_add_f32 v[18:19], v[234:235], v[18:19]
	v_pk_add_f32 v[20:21], v[236:237], v[20:21]
	v_pk_add_f32 v[22:23], v[238:239], v[22:23]
	v_pk_add_f32 v[24:25], v[240:241], v[24:25]
	v_pk_add_f32 v[26:27], v[106:107], v[26:27]
	v_pk_add_f32 v[28:29], v[108:109], v[28:29]
	v_pk_add_f32 v[30:31], v[110:111], v[30:31]
	v_pk_add_f32 v[32:33], v[112:113], v[32:33]
	v_fma_mix_f32 v206, v234, v122, v206 op_sel:[0,0,0] op_sel_hi:[0,1,0]
	v_fma_mix_f32 v207, v235, v122, v207 op_sel:[0,1,0] op_sel_hi:[0,1,0]
	v_fma_mix_f32 v200, v236, v123, v200 op_sel:[0,0,0] op_sel_hi:[0,1,0]
	v_fma_mix_f32 v201, v237, v123, v201 op_sel:[0,1,0] op_sel_hi:[0,1,0]
	v_fma_mix_f32 v198, v238, v124, v198 op_sel:[0,0,0] op_sel_hi:[0,1,0]
	v_fma_mix_f32 v199, v239, v124, v199 op_sel:[0,1,0] op_sel_hi:[0,1,0]
	v_fma_mix_f32 v194, v240, v125, v194 op_sel:[0,0,0] op_sel_hi:[0,1,0]
	v_fma_mix_f32 v195, v241, v125, v195 op_sel:[0,1,0] op_sel_hi:[0,1,0]
	v_fma_mix_f32 v192, v106, v182, v192 op_sel:[0,0,0] op_sel_hi:[0,1,0]
	v_fma_mix_f32 v193, v107, v182, v193 op_sel:[0,1,0] op_sel_hi:[0,1,0]
	v_fma_mix_f32 v190, v108, v183, v190 op_sel:[0,0,0] op_sel_hi:[0,1,0]
	v_fma_mix_f32 v191, v109, v183, v191 op_sel:[0,1,0] op_sel_hi:[0,1,0]
	v_fma_mix_f32 v188, v110, v184, v188 op_sel:[0,0,0] op_sel_hi:[0,1,0]
	v_fma_mix_f32 v189, v111, v184, v189 op_sel:[0,1,0] op_sel_hi:[0,1,0]
	v_fma_mix_f32 v186, v112, v185, v186 op_sel:[0,0,0] op_sel_hi:[0,1,0]
	v_fma_mix_f32 v187, v113, v185, v187 op_sel:[0,1,0] op_sel_hi:[0,1,0]
	s_setprio 0
	s_addk_i32 s4, 0x280
	s_cmpk_eq_i32 s4, 0x2080
	s_cbranch_scc0 .LBB1_14
	s_waitcnt lgkmcnt(0)

	.amdhsa_kernel _Z11main_kernelPKcPf
		.amdhsa_group_segment_fixed_size 147456
		.amdhsa_private_segment_fixed_size 0
		.amdhsa_kernarg_size 16
		.amdhsa_user_sgpr_count 2
		.amdhsa_user_sgpr_dispatch_ptr 0
		.amdhsa_user_sgpr_queue_ptr 0
		.amdhsa_user_sgpr_kernarg_segment_ptr 1
		.amdhsa_user_sgpr_dispatch_id 0
		.amdhsa_user_sgpr_kernarg_preload_length 0
		.amdhsa_user_sgpr_kernarg_preload_offset 0
		.amdhsa_user_sgpr_private_segment_size 0
		.amdhsa_uses_dynamic_stack 0
		.amdhsa_enable_private_segment 0
		.amdhsa_system_sgpr_workgroup_id_x 1
		.amdhsa_system_sgpr_workgroup_id_y 0
		.amdhsa_system_sgpr_workgroup_id_z 0
		.amdhsa_system_sgpr_workgroup_info 0
		.amdhsa_system_vgpr_workitem_id 0
		.amdhsa_next_free_vgpr 256
		.amdhsa_next_free_sgpr 96
		.amdhsa_accum_offset 256
		.amdhsa_reserve_vcc 1
		.amdhsa_float_round_mode_32 0
		.amdhsa_float_round_mode_16_64 0
		.amdhsa_float_denorm_mode_32 3
		.amdhsa_float_denorm_mode_16_64 3
		.amdhsa_dx10_clamp 1
		.amdhsa_ieee_mode 1
		.amdhsa_fp16_overflow 0
		.amdhsa_tg_split 0
		.amdhsa_exception_fp_ieee_invalid_op 0
		.amdhsa_exception_fp_denorm_src 0
		.amdhsa_exception_fp_ieee_div_zero 0
		.amdhsa_exception_fp_ieee_overflow 0
		.amdhsa_exception_fp_ieee_underflow 0
		.amdhsa_exception_fp_ieee_inexact 0
		.amdhsa_exception_int_div_zero 0
	.end_amdhsa_kernel

amdhsa.kernels:
  - .agpr_count:     32
    .args:
      - .actual_access:  read_only
        .address_space:  global
        .offset:         0
        .size:           8
        .value_kind:     global_buffer
      - .actual_access:  read_only
        .address_space:  global
        .offset:         8
        .size:           8
        .value_kind:     global_buffer
      - .actual_access:  read_only
        .address_space:  global
        .offset:         16
        .size:           8
        .value_kind:     global_buffer
      - .actual_access:  read_only
        .address_space:  global
        .offset:         24
        .size:           8
        .value_kind:     global_buffer
      - .actual_access:  read_only
        .address_space:  global
        .offset:         32
        .size:           8
        .value_kind:     global_buffer
      - .actual_access:  read_only
        .address_space:  global
        .offset:         40
        .size:           8
        .value_kind:     global_buffer
      - .actual_access:  read_only
        .address_space:  global
        .offset:         48
        .size:           8
        .value_kind:     global_buffer
      - .actual_access:  read_only
        .address_space:  global
        .offset:         56
        .size:           8
        .value_kind:     global_buffer
      - .actual_access:  read_only
        .address_space:  global
        .offset:         64
        .size:           8
        .value_kind:     global_buffer
      - .actual_access:  read_only
        .address_space:  global
        .offset:         72
        .size:           8
        .value_kind:     global_buffer
      - .actual_access:  read_only
        .address_space:  global
        .offset:         80
        .size:           8
        .value_kind:     global_buffer
      - .actual_access:  read_only
        .address_space:  global
        .offset:         88
        .size:           8
        .value_kind:     global_buffer
      - .actual_access:  read_only
        .address_space:  global
        .offset:         96
        .size:           8
        .value_kind:     global_buffer
      - .actual_access:  read_only
        .address_space:  global
        .offset:         104
        .size:           8
        .value_kind:     global_buffer
      - .actual_access:  read_only
        .address_space:  global
        .offset:         112
        .size:           8
        .value_kind:     global_buffer
      - .actual_access:  read_only
        .address_space:  global
        .offset:         120
        .size:           8
        .value_kind:     global_buffer
      - .actual_access:  read_only
        .address_space:  global
        .offset:         128
        .size:           8
        .value_kind:     global_buffer
      - .actual_access:  read_only
        .address_space:  global
        .offset:         136
        .size:           8
        .value_kind:     global_buffer
      - .actual_access:  read_only
        .address_space:  global
        .offset:         144
        .size:           8
        .value_kind:     global_buffer
      - .actual_access:  read_only
        .address_space:  global
        .offset:         152
        .size:           8
        .value_kind:     global_buffer
      - .actual_access:  read_only
        .address_space:  global
        .offset:         160
        .size:           8
        .value_kind:     global_buffer
      - .actual_access:  read_only
        .address_space:  global
        .offset:         168
        .size:           8
        .value_kind:     global_buffer
      - .actual_access:  write_only
        .address_space:  global
        .offset:         176
        .size:           8
        .value_kind:     global_buffer
    .group_segment_fixed_size: 0
    .kernarg_segment_align: 8
    .kernarg_segment_size: 184
    .language:       OpenCL C
    .language_version:
      - 2
      - 0
    .max_flat_workgroup_size: 256
    .name:           _Z11prep_kernelPKfS0_S0_S0_S0_S0_S0_S0_S0_S0_S0_S0_S0_S0_S0_S0_S0_S0_S0_S0_S0_S0_Pc
    .private_segment_fixed_size: 0
    .sgpr_count:     32
    .sgpr_spill_count: 0
    .symbol:         _Z11prep_kernelPKfS0_S0_S0_S0_S0_S0_S0_S0_S0_S0_S0_S0_S0_S0_S0_S0_S0_S0_S0_S0_S0_Pc.kd
    .uniform_work_group_size: 1
    .uses_dynamic_stack: false
    .vgpr_count:     272
    .vgpr_spill_count: 0
    .wavefront_size: 64
  - .agpr_count:     0
    .args:
      - .actual_access:  read_only
        .address_space:  global
        .offset:         0
        .size:           8
        .value_kind:     global_buffer
      - .actual_access:  write_only
        .address_space:  global
        .offset:         8
        .size:           8
        .value_kind:     global_buffer
    .group_segment_fixed_size: 147456
    .kernarg_segment_align: 8
    .kernarg_segment_size: 16
    .language:       OpenCL C
    .language_version:
      - 2
      - 0
    .max_flat_workgroup_size: 512
    .name:           _Z11main_kernelPKcPf
    .private_segment_fixed_size: 0
    .sgpr_count:     28
    .sgpr_spill_count: 0
    .symbol:         _Z11main_kernelPKcPf.kd
    .uniform_work_group_size: 1
    .uses_dynamic_stack: false
    .vgpr_count:     256
    .vgpr_spill_count: 0
    .wavefront_size: 64
  - .agpr_count:     0
    .args:
      - .actual_access:  read_only
        .address_space:  global
        .offset:         0
        .size:           8
        .value_kind:     global_buffer
      - .actual_access:  read_only
        .address_space:  global
        .offset:         8
        .size:           8
        .value_kind:     global_buffer
      - .actual_access:  read_only
        .address_space:  global
        .offset:         16
        .size:           8
        .value_kind:     global_buffer
      - .actual_access:  read_only
        .address_space:  global
        .offset:         24
        .size:           8
        .value_kind:     global_buffer
      - .actual_access:  read_only
        .address_space:  global
        .offset:         32
        .size:           8
        .value_kind:     global_buffer
      - .actual_access:  read_only
        .address_space:  global
        .offset:         40
        .size:           8
        .value_kind:     global_buffer
      - .actual_access:  read_only
        .address_space:  global
        .offset:         48
        .size:           8
        .value_kind:     global_buffer
      - .actual_access:  read_only
        .address_space:  global
        .offset:         56
        .size:           8
        .value_kind:     global_buffer
      - .actual_access:  read_only
        .address_space:  global
        .offset:         64
        .size:           8
        .value_kind:     global_buffer
      - .actual_access:  read_only
        .address_space:  global
        .offset:         72
        .size:           8
        .value_kind:     global_buffer
      - .actual_access:  read_only
        .address_space:  global
        .offset:         80
        .size:           8
        .value_kind:     global_buffer
      - .actual_access:  write_only
        .address_space:  global
        .offset:         88
        .size:           8
        .value_kind:     global_buffer
    .group_segment_fixed_size: 1536
    .kernarg_segment_align: 8
    .kernarg_segment_size: 96
    .language:       OpenCL C
    .language_version:
      - 2
      - 0
    .max_flat_workgroup_size: 128
    .name:           _Z12final_kernelPKfS0_S0_S0_S0_S0_S0_S0_S0_S0_S0_Pf
    .private_segment_fixed_size: 0
    .sgpr_count:     30
    .sgpr_spill_count: 0
    .symbol:         _Z12final_kernelPKfS0_S0_S0_S0_S0_S0_S0_S0_S0_S0_Pf.kd
    .uniform_work_group_size: 1
    .uses_dynamic_stack: false
    .vgpr_count:     159
    .vgpr_spill_count: 0
    .wavefront_size: 64
